# in-proj GEMM loop: four of the six LDS-DMA pieces of each 6-piece load segment issued between the MFMAs of the wave's own compute segment (counted wait 8 -> 4)
# baseline (speedup 1.0000x reference)
.LBB0_213:
	s_add_u32 s14, s12, 0xfffc0080
	s_addc_u32 s15, s13, -1
	s_add_i32 s36, 0, 0x10000
	s_cmp_eq_u32 s29, 12
	s_cselect_b32 s17, s9, s15
	s_cselect_b32 s16, s8, s14
	s_cselect_b32 s15, s11, s28
	s_cselect_b32 s14, s10, s7
	s_add_i32 s42, 0, 0x14000
	v_add_u32_e32 v158, s36, v147
	v_add_u32_e32 v174, s42, v147
	ds_read_b128 v[142:145], v158
	ds_read_b128 v[150:153], v158 offset:1024
	ds_read_b128 v[154:157], v158 offset:2048
	ds_read_b128 v[158:161], v158 offset:3072
	ds_read_b128 v[162:165], v174
	ds_read_b128 v[166:169], v174 offset:1024
	ds_read_b128 v[170:173], v174 offset:2048
	ds_read_b128 v[174:177], v174 offset:3072
	v_lshl_add_u64 v[190:191], s[12:13], 0, v[138:139]
	s_add_i32 m0, s19, 0xc000
	ds_read_b128 v[178:181], v149
	ds_read_b128 v[182:185], v149 offset:1024
	ds_read_b128 v[186:189], v149 offset:2048
	ds_read_b128 v[198:201], v149 offset:3072
	ds_read_b128 v[202:205], v149 offset:4096
	ds_read_b128 v[206:209], v149 offset:5120
	ds_read_b128 v[210:213], v149 offset:6144
	ds_read_b128 v[214:217], v149 offset:7168
	global_load_lds_dwordx4 v[190:191], off
	v_lshl_add_u64 v[190:191], s[12:13], 0, v[140:141]
	s_add_i32 m0, s19, 0xe000
	s_nop 0
	global_load_lds_dwordx4 v[190:191], off
	s_waitcnt vmcnt(8)
	s_waitcnt lgkmcnt(0)
	s_barrier
	s_setprio 1
	s_waitcnt lgkmcnt(0)
	v_mfma_f32_16x16x32_bf16 v[126:129], v[142:145], v[178:181], v[126:129]
	v_mfma_f32_16x16x32_bf16 v[122:125], v[154:157], v[178:181], v[122:125]
	v_mfma_f32_16x16x32_bf16 v[110:113], v[142:145], v[186:189], v[110:113]
	v_mfma_f32_16x16x32_bf16 v[106:109], v[154:157], v[186:189], v[106:109]
	v_mfma_f32_16x16x32_bf16 v[94:97], v[142:145], v[202:205], v[94:97]
	v_mfma_f32_16x16x32_bf16 v[90:93], v[154:157], v[202:205], v[90:93]
	v_mfma_f32_16x16x32_bf16 v[78:81], v[142:145], v[210:213], v[78:81]
	v_mfma_f32_16x16x32_bf16 v[74:77], v[154:157], v[210:213], v[74:77]
	v_mfma_f32_16x16x32_bf16 v[126:129], v[150:153], v[182:185], v[126:129]
	v_mfma_f32_16x16x32_bf16 v[122:125], v[158:161], v[182:185], v[122:125]
	v_mfma_f32_16x16x32_bf16 v[110:113], v[150:153], v[198:201], v[110:113]
	v_mfma_f32_16x16x32_bf16 v[106:109], v[158:161], v[198:201], v[106:109]
	v_mfma_f32_16x16x32_bf16 v[94:97], v[150:153], v[206:209], v[94:97]
	v_mfma_f32_16x16x32_bf16 v[90:93], v[158:161], v[206:209], v[90:93]
	v_mfma_f32_16x16x32_bf16 v[78:81], v[150:153], v[214:217], v[78:81]
	v_mfma_f32_16x16x32_bf16 v[74:77], v[158:161], v[214:217], v[74:77]
	s_setprio 0
	s_setprio 1
	v_mfma_f32_16x16x32_bf16 v[118:121], v[162:165], v[178:181], v[118:121]
	v_mfma_f32_16x16x32_bf16 v[114:117], v[170:173], v[178:181], v[114:117]
	v_mfma_f32_16x16x32_bf16 v[102:105], v[162:165], v[186:189], v[102:105]
	v_mfma_f32_16x16x32_bf16 v[98:101], v[170:173], v[186:189], v[98:101]
	v_mfma_f32_16x16x32_bf16 v[86:89], v[162:165], v[202:205], v[86:89]
	v_mfma_f32_16x16x32_bf16 v[82:85], v[170:173], v[202:205], v[82:85]
	v_mfma_f32_16x16x32_bf16 v[70:73], v[162:165], v[210:213], v[70:73]
	v_mfma_f32_16x16x32_bf16 v[66:69], v[170:173], v[210:213], v[66:69]
	v_mfma_f32_16x16x32_bf16 v[118:121], v[166:169], v[182:185], v[118:121]
	v_mfma_f32_16x16x32_bf16 v[114:117], v[174:177], v[182:185], v[114:117]
	v_mfma_f32_16x16x32_bf16 v[102:105], v[166:169], v[198:201], v[102:105]
	v_mfma_f32_16x16x32_bf16 v[98:101], v[174:177], v[198:201], v[98:101]
	v_mfma_f32_16x16x32_bf16 v[86:89], v[166:169], v[206:209], v[86:89]
	v_mfma_f32_16x16x32_bf16 v[82:85], v[174:177], v[206:209], v[82:85]
	v_mfma_f32_16x16x32_bf16 v[70:73], v[166:169], v[214:217], v[70:73]
	v_mfma_f32_16x16x32_bf16 v[66:69], v[174:177], v[214:217], v[66:69]
	s_setprio 0
	s_barrier
	s_add_i32 s36, s36, s18
	v_lshl_add_u64 v[190:191], s[14:15], 0, v[130:131]
	s_mov_b32 m0, s36
	ds_read_b128 v[178:181], v149 offset:16384
	ds_read_b128 v[182:185], v149 offset:17408
	ds_read_b128 v[186:189], v149 offset:18432
	ds_read_b128 v[198:201], v149 offset:19456
	ds_read_b128 v[202:205], v149 offset:20480
	ds_read_b128 v[206:209], v149 offset:21504
	ds_read_b128 v[210:213], v149 offset:22528
	ds_read_b128 v[214:217], v149 offset:23552
	global_load_lds_dwordx4 v[190:191], off
	s_add_i32 m0, s36, 0x2000
	s_add_u32 s36, s14, 0x40000
	v_lshl_add_u64 v[218:219], s[14:15], 0, v[132:133]
	s_addc_u32 s37, s15, 0
	s_add_i32 s42, s42, s18
	global_load_lds_dwordx4 v[218:219], off
	s_waitcnt vmcnt(4)
	s_waitcnt lgkmcnt(0)
	s_barrier
	s_setprio 1
	s_waitcnt lgkmcnt(0)
	v_mfma_f32_16x16x32_bf16 v[62:65], v[142:145], v[178:181], v[62:65]
	v_mfma_f32_16x16x32_bf16 v[58:61], v[154:157], v[178:181], v[58:61]
	v_mfma_f32_16x16x32_bf16 v[46:49], v[142:145], v[186:189], v[46:49]
	v_lshl_add_u64 v[220:221], s[36:37], 0, v[130:131]
	s_mov_b32 m0, s42
	v_lshl_add_u64 v[222:223], s[16:17], 0, v[134:135]
	v_mfma_f32_16x16x32_bf16 v[42:45], v[154:157], v[186:189], v[42:45]
	global_load_lds_dwordx4 v[220:221], off
	v_mfma_f32_16x16x32_bf16 v[30:33], v[142:145], v[202:205], v[30:33]
	v_mfma_f32_16x16x32_bf16 v[26:29], v[154:157], v[202:205], v[26:29]
	v_mfma_f32_16x16x32_bf16 v[14:17], v[142:145], v[210:213], v[14:17]
	v_mfma_f32_16x16x32_bf16 v[10:13], v[154:157], v[210:213], v[10:13]
	v_mfma_f32_16x16x32_bf16 v[62:65], v[150:153], v[182:185], v[62:65]
	v_mfma_f32_16x16x32_bf16 v[58:61], v[158:161], v[182:185], v[58:61]
	v_lshl_add_u64 v[220:221], s[36:37], 0, v[132:133]
	s_add_i32 m0, s42, 0x2000
	v_mfma_f32_16x16x32_bf16 v[46:49], v[150:153], v[198:201], v[46:49]
	global_load_lds_dwordx4 v[220:221], off
	v_mfma_f32_16x16x32_bf16 v[42:45], v[158:161], v[198:201], v[42:45]
	v_mfma_f32_16x16x32_bf16 v[30:33], v[150:153], v[206:209], v[30:33]
	v_mfma_f32_16x16x32_bf16 v[26:29], v[158:161], v[206:209], v[26:29]
	v_mfma_f32_16x16x32_bf16 v[14:17], v[150:153], v[214:217], v[14:17]
	v_mfma_f32_16x16x32_bf16 v[10:13], v[158:161], v[214:217], v[10:13]
	s_setprio 0
	s_setprio 1
	v_mfma_f32_16x16x32_bf16 v[54:57], v[162:165], v[178:181], v[54:57]
	v_mfma_f32_16x16x32_bf16 v[50:53], v[170:173], v[178:181], v[50:53]
	v_lshl_add_u64 v[220:221], s[16:17], 0, v[136:137]
	s_mov_b32 m0, s19
	v_mfma_f32_16x16x32_bf16 v[38:41], v[162:165], v[186:189], v[38:41]
	global_load_lds_dwordx4 v[220:221], off
	v_mfma_f32_16x16x32_bf16 v[34:37], v[170:173], v[186:189], v[34:37]
	v_mfma_f32_16x16x32_bf16 v[22:25], v[162:165], v[202:205], v[22:25]
	v_mfma_f32_16x16x32_bf16 v[18:21], v[170:173], v[202:205], v[18:21]
	v_mfma_f32_16x16x32_bf16 v[6:9], v[162:165], v[210:213], v[6:9]
	v_mfma_f32_16x16x32_bf16 v[2:5], v[170:173], v[210:213], v[2:5]
	v_mfma_f32_16x16x32_bf16 v[54:57], v[166:169], v[182:185], v[54:57]
	v_mfma_f32_16x16x32_bf16 v[50:53], v[174:177], v[182:185], v[50:53]
	s_mov_b32 m0, s20
	v_mfma_f32_16x16x32_bf16 v[38:41], v[166:169], v[198:201], v[38:41]
	global_load_lds_dwordx4 v[222:223], off
	v_mfma_f32_16x16x32_bf16 v[34:37], v[174:177], v[198:201], v[34:37]
	v_mfma_f32_16x16x32_bf16 v[22:25], v[166:169], v[206:209], v[22:25]
	v_mfma_f32_16x16x32_bf16 v[18:21], v[174:177], v[206:209], v[18:21]
	v_mfma_f32_16x16x32_bf16 v[6:9], v[166:169], v[214:217], v[6:9]
	v_mfma_f32_16x16x32_bf16 v[2:5], v[174:177], v[214:217], v[2:5]
	s_setprio 0
	s_barrier
	s_add_i32 s36, 0, 0x18000
	s_add_i32 s37, 0, 0x1c000
	v_add_u32_e32 v158, s36, v147
	v_add_u32_e32 v174, s37, v147
	ds_read_b128 v[142:145], v158
	ds_read_b128 v[150:153], v158 offset:1024
	ds_read_b128 v[154:157], v158 offset:2048
	ds_read_b128 v[158:161], v158 offset:3072
	ds_read_b128 v[162:165], v174
	ds_read_b128 v[166:169], v174 offset:1024
	ds_read_b128 v[170:173], v174 offset:2048
	ds_read_b128 v[174:177], v174 offset:3072
	s_add_u32 s16, s16, 0x40000
	s_addc_u32 s17, s17, 0
	s_mov_b32 m0, s21
	v_lshl_add_u64 v[224:225], s[16:17], 0, v[136:137]
	ds_read_b128 v[178:181], v149 offset:32768
	ds_read_b128 v[182:185], v149 offset:33792
	ds_read_b128 v[186:189], v149 offset:34816
	ds_read_b128 v[198:201], v149 offset:35840
	ds_read_b128 v[202:205], v149 offset:36864
	ds_read_b128 v[206:209], v149 offset:37888
	ds_read_b128 v[210:213], v149 offset:38912
	ds_read_b128 v[214:217], v149 offset:39936
	global_load_lds_dwordx4 v[224:225], off
	v_lshl_add_u64 v[224:225], s[16:17], 0, v[134:135]
	s_mov_b32 m0, s22
	s_nop 0
	global_load_lds_dwordx4 v[224:225], off
	s_waitcnt vmcnt(8)
	s_waitcnt lgkmcnt(0)
	s_barrier
	s_setprio 1
	s_waitcnt lgkmcnt(0)
	v_mfma_f32_16x16x32_bf16 v[126:129], v[142:145], v[178:181], v[126:129]
	v_mfma_f32_16x16x32_bf16 v[122:125], v[154:157], v[178:181], v[122:125]
	v_mfma_f32_16x16x32_bf16 v[110:113], v[142:145], v[186:189], v[110:113]
	v_mfma_f32_16x16x32_bf16 v[106:109], v[154:157], v[186:189], v[106:109]
	v_mfma_f32_16x16x32_bf16 v[94:97], v[142:145], v[202:205], v[94:97]
	v_mfma_f32_16x16x32_bf16 v[90:93], v[154:157], v[202:205], v[90:93]
	v_mfma_f32_16x16x32_bf16 v[78:81], v[142:145], v[210:213], v[78:81]
	v_mfma_f32_16x16x32_bf16 v[74:77], v[154:157], v[210:213], v[74:77]
	v_mfma_f32_16x16x32_bf16 v[126:129], v[150:153], v[182:185], v[126:129]
	v_mfma_f32_16x16x32_bf16 v[122:125], v[158:161], v[182:185], v[122:125]
	v_mfma_f32_16x16x32_bf16 v[110:113], v[150:153], v[198:201], v[110:113]
	v_mfma_f32_16x16x32_bf16 v[106:109], v[158:161], v[198:201], v[106:109]
	v_mfma_f32_16x16x32_bf16 v[94:97], v[150:153], v[206:209], v[94:97]
	v_mfma_f32_16x16x32_bf16 v[90:93], v[158:161], v[206:209], v[90:93]
	v_mfma_f32_16x16x32_bf16 v[78:81], v[150:153], v[214:217], v[78:81]
	v_mfma_f32_16x16x32_bf16 v[74:77], v[158:161], v[214:217], v[74:77]
	s_setprio 0
	s_setprio 1
	v_mfma_f32_16x16x32_bf16 v[118:121], v[162:165], v[178:181], v[118:121]
	v_mfma_f32_16x16x32_bf16 v[114:117], v[170:173], v[178:181], v[114:117]
	v_mfma_f32_16x16x32_bf16 v[102:105], v[162:165], v[186:189], v[102:105]
	v_mfma_f32_16x16x32_bf16 v[98:101], v[170:173], v[186:189], v[98:101]
	v_mfma_f32_16x16x32_bf16 v[86:89], v[162:165], v[202:205], v[86:89]
	v_mfma_f32_16x16x32_bf16 v[82:85], v[170:173], v[202:205], v[82:85]
	v_mfma_f32_16x16x32_bf16 v[70:73], v[162:165], v[210:213], v[70:73]
	v_mfma_f32_16x16x32_bf16 v[66:69], v[170:173], v[210:213], v[66:69]
	v_mfma_f32_16x16x32_bf16 v[118:121], v[166:169], v[182:185], v[118:121]
	v_mfma_f32_16x16x32_bf16 v[114:117], v[174:177], v[182:185], v[114:117]
	v_mfma_f32_16x16x32_bf16 v[102:105], v[166:169], v[198:201], v[102:105]
	v_mfma_f32_16x16x32_bf16 v[98:101], v[174:177], v[198:201], v[98:101]
	v_mfma_f32_16x16x32_bf16 v[86:89], v[166:169], v[206:209], v[86:89]
	v_mfma_f32_16x16x32_bf16 v[82:85], v[174:177], v[206:209], v[82:85]
	v_mfma_f32_16x16x32_bf16 v[70:73], v[166:169], v[214:217], v[70:73]
	v_mfma_f32_16x16x32_bf16 v[66:69], v[174:177], v[214:217], v[66:69]
	s_setprio 0
	s_barrier
	s_add_i32 s16, s36, s18
	v_lshl_add_u64 v[190:191], v[190:191], 0, s[84:85]
	s_mov_b32 m0, s16
	ds_read_b128 v[178:181], v149 offset:49152
	ds_read_b128 v[182:185], v149 offset:50176
	ds_read_b128 v[186:189], v149 offset:51200
	ds_read_b128 v[198:201], v149 offset:52224
	ds_read_b128 v[202:205], v149 offset:53248
	ds_read_b128 v[206:209], v149 offset:54272
	ds_read_b128 v[210:213], v149 offset:55296
	ds_read_b128 v[214:217], v149 offset:56320
	global_load_lds_dwordx4 v[190:191], off
	s_add_i32 m0, s16, 0x2000
	s_add_u32 s14, s14, 0x40080
	v_lshl_add_u64 v[190:191], v[218:219], 0, s[84:85]
	s_addc_u32 s15, s15, 0
	s_add_i32 s16, s37, s18
	global_load_lds_dwordx4 v[190:191], off
	s_waitcnt vmcnt(4)
	s_waitcnt lgkmcnt(0)
	s_barrier
	s_setprio 1
	s_waitcnt lgkmcnt(0)
	v_mfma_f32_16x16x32_bf16 v[62:65], v[142:145], v[178:181], v[62:65]
	v_mfma_f32_16x16x32_bf16 v[58:61], v[154:157], v[178:181], v[58:61]
	v_mfma_f32_16x16x32_bf16 v[46:49], v[142:145], v[186:189], v[46:49]
	v_lshl_add_u64 v[190:191], s[14:15], 0, v[130:131]
	s_mov_b32 m0, s16
	v_mfma_f32_16x16x32_bf16 v[42:45], v[154:157], v[186:189], v[42:45]
	global_load_lds_dwordx4 v[190:191], off
	v_mfma_f32_16x16x32_bf16 v[30:33], v[142:145], v[202:205], v[30:33]
	v_mfma_f32_16x16x32_bf16 v[26:29], v[154:157], v[202:205], v[26:29]
	v_mfma_f32_16x16x32_bf16 v[14:17], v[142:145], v[210:213], v[14:17]
	v_mfma_f32_16x16x32_bf16 v[10:13], v[154:157], v[210:213], v[10:13]
	v_mfma_f32_16x16x32_bf16 v[62:65], v[150:153], v[182:185], v[62:65]
	v_mfma_f32_16x16x32_bf16 v[58:61], v[158:161], v[182:185], v[58:61]
	v_lshl_add_u64 v[190:191], s[14:15], 0, v[132:133]
	s_add_i32 m0, s16, 0x2000
	v_mfma_f32_16x16x32_bf16 v[46:49], v[150:153], v[198:201], v[46:49]
	global_load_lds_dwordx4 v[190:191], off
	v_mfma_f32_16x16x32_bf16 v[42:45], v[158:161], v[198:201], v[42:45]
	v_mfma_f32_16x16x32_bf16 v[30:33], v[150:153], v[206:209], v[30:33]
	v_mfma_f32_16x16x32_bf16 v[26:29], v[158:161], v[206:209], v[26:29]
	v_mfma_f32_16x16x32_bf16 v[14:17], v[150:153], v[214:217], v[14:17]
	v_mfma_f32_16x16x32_bf16 v[10:13], v[158:161], v[214:217], v[10:13]
	s_setprio 0
	s_setprio 1
	v_mfma_f32_16x16x32_bf16 v[54:57], v[162:165], v[178:181], v[54:57]
	v_mfma_f32_16x16x32_bf16 v[50:53], v[170:173], v[178:181], v[50:53]
	v_lshl_add_u64 v[190:191], v[220:221], 0, s[84:85]
	s_mov_b32 m0, s23
	v_mfma_f32_16x16x32_bf16 v[38:41], v[162:165], v[186:189], v[38:41]
	global_load_lds_dwordx4 v[190:191], off
	v_mfma_f32_16x16x32_bf16 v[34:37], v[170:173], v[186:189], v[34:37]
	v_mfma_f32_16x16x32_bf16 v[22:25], v[162:165], v[202:205], v[22:25]
	v_mfma_f32_16x16x32_bf16 v[18:21], v[170:173], v[202:205], v[18:21]
	v_mfma_f32_16x16x32_bf16 v[6:9], v[162:165], v[210:213], v[6:9]
	v_mfma_f32_16x16x32_bf16 v[2:5], v[170:173], v[210:213], v[2:5]
	v_mfma_f32_16x16x32_bf16 v[54:57], v[166:169], v[182:185], v[54:57]
	v_mfma_f32_16x16x32_bf16 v[50:53], v[174:177], v[182:185], v[50:53]
	v_lshl_add_u64 v[190:191], v[222:223], 0, s[84:85]
	s_mov_b32 m0, s24
	v_mfma_f32_16x16x32_bf16 v[38:41], v[166:169], v[198:201], v[38:41]
	global_load_lds_dwordx4 v[190:191], off
	v_mfma_f32_16x16x32_bf16 v[34:37], v[174:177], v[198:201], v[34:37]
	v_mfma_f32_16x16x32_bf16 v[22:25], v[166:169], v[206:209], v[22:25]
	v_mfma_f32_16x16x32_bf16 v[18:21], v[174:177], v[206:209], v[18:21]
	v_mfma_f32_16x16x32_bf16 v[6:9], v[166:169], v[214:217], v[6:9]
	v_mfma_f32_16x16x32_bf16 v[2:5], v[174:177], v[214:217], v[2:5]
	s_setprio 0
	s_barrier
	s_add_i32 s29, s29, 2
	s_add_u32 s12, s12, 0x100
	s_addc_u32 s13, s13, 0
	s_add_u32 s7, s7, 0x100
	s_addc_u32 s28, s28, 0
	s_cmp_gt_u32 s29, 13
	s_cbranch_scc0 .LBB0_213
	s_and_b64 vcc, exec, s[4:5]
	s_cbranch_vccz .LBB0_216
	s_barrier
